# as nt11 plus: table-hook f32 chunks loaded straight into the converter VGPRs (nt) instead of LDS-DMA + ds_read round trip
# baseline (speedup 1.0000x reference)
; #define PG8_LAS __attribute__((address_space(3)))
; __device__ __forceinline__ void hook_issue(const TblHook& h, int it, int lane, PG8_LAS unsigned char* slot) {
;     const int q = __builtin_amdgcn_readfirstlane(it * h.ngw + h.gwave); const int qq = q < HK_NCHUNK ? q : 0; const bool isu = qq < HK_HALF; const int j = isu ? qq : qq - HK_HALF;
;     const __amdgpu_buffer_rsrc_t r = __builtin_amdgcn_make_buffer_rsrc((void*)(isu ? h.u : h.v), (short)0, 0x7fffffff, 0x00020000);
;     const unsigned so = (unsigned)j * 2048u, l16 = (unsigned)lane * 16u;
;     __builtin_amdgcn_raw_ptr_buffer_load_lds(r, (PG8_LAS void*)slot, 16, l16, so, 0, 0);
;     __builtin_amdgcn_raw_ptr_buffer_load_lds(r, (PG8_LAS void*)(slot + 1024), 16, l16, so + 1024u, 0, 0);
; }
.LBB0_183:
	s_andn2_b64 vcc, exec, s[4:5]
	s_mul_i32 s40, s43, s42
	s_cbranch_vccnz .LBB0_185
	s_add_i32 s4, s40, s12
	s_cmp_lt_i32 s4, 0x40000
	s_cselect_b32 s41, s4, 0
	s_cmp_lt_i32 s41, 0x20000
	s_cselect_b64 s[26:27], -1, 0
	s_and_b64 s[4:5], s[26:27], exec
	s_cselect_b32 s4, s58, s60
	s_cselect_b32 s5, s59, s61
	s_lshl_b32 s41, s41, 11
	s_and_b32 s5, s5, 0xffff
	s_add_i32 s93, s41, 0xf0000000
	s_and_b64 s[26:27], s[26:27], exec
	s_mov_b32 m0, s74
	s_cselect_b32 s26, s41, s93
	buffer_load_dwordx4 v[198:201], v214, s[4:7], s26 offen nt
	s_bitset1_b32 s26, 10
	s_mov_b32 m0, s75
	s_nop 0
	buffer_load_dwordx4 v[194:197], v214, s[4:7], s26 offen nt
	s_waitcnt vmcnt(10)

; __device__ __forceinline__ void hook_store(const TblHook& h, int it, int lane, const f32x4 a, const f32x4 b) {
;     const int q = __builtin_amdgcn_readfirstlane(it * h.ngw + h.gwave); const bool act = q < HK_NCHUNK; const int qq = act ? q : 0;
;     const bool isu = qq < HK_HALF; const int j = isu ? qq : qq - HK_HALF; const int e = j >> 3, c512 = j & 7, sl = c512 >> 1, c0 = (c512 & 1) * 512;
;     unsigned char* dt = h.ub + (isu ? (size_t)0 : ((size_t)64 << 20)) + ((size_t)sl * 16384 + e) * 1024 + c0;
.LBB0_193:
	s_waitcnt lgkmcnt(0)
	s_bitset1_b32 s93, 7
	s_or_b32 s4, s41, 0x80
	s_barrier
	s_setprio 1
	s_waitcnt lgkmcnt(7)
	v_mfma_i32_16x16x64_i8 v[142:145], v[158:161], v[190:193], v[142:145]
	s_waitcnt lgkmcnt(6)
	v_mfma_i32_16x16x64_i8 v[142:145], v[154:157], v[186:189], v[142:145]
	v_mfma_i32_16x16x64_i8 v[138:141], v[150:153], v[190:193], v[138:141]
	s_nop 0
	v_mfma_i32_16x16x64_i8 v[138:141], v[146:149], v[186:189], v[138:141]
	s_waitcnt lgkmcnt(5)
	v_mfma_i32_16x16x64_i8 v[126:129], v[158:161], v[182:185], v[126:129]
	s_waitcnt lgkmcnt(4)
	v_mfma_i32_16x16x64_i8 v[126:129], v[154:157], v[178:181], v[126:129]
	v_mfma_i32_16x16x64_i8 v[122:125], v[150:153], v[182:185], v[122:125]
	s_nop 0
	v_mfma_i32_16x16x64_i8 v[122:125], v[146:149], v[178:181], v[122:125]
	s_waitcnt lgkmcnt(3)
	v_mfma_i32_16x16x64_i8 v[94:97], v[158:161], v[174:177], v[94:97]
	s_waitcnt lgkmcnt(2)
	v_mfma_i32_16x16x64_i8 v[94:97], v[154:157], v[170:173], v[94:97]
	v_mfma_i32_16x16x64_i8 v[90:93], v[150:153], v[174:177], v[90:93]
	s_nop 0
	v_mfma_i32_16x16x64_i8 v[90:93], v[146:149], v[170:173], v[90:93]
	s_waitcnt lgkmcnt(1)
	v_mfma_i32_16x16x64_i8 v[78:81], v[158:161], v[166:169], v[78:81]
	s_waitcnt lgkmcnt(0)
	v_mfma_i32_16x16x64_i8 v[78:81], v[154:157], v[162:165], v[78:81]
	v_mfma_i32_16x16x64_i8 v[74:77], v[150:153], v[166:169], v[74:77]
	s_nop 0
	v_mfma_i32_16x16x64_i8 v[74:77], v[146:149], v[162:165], v[74:77]
	s_setprio 0
	s_setprio 1
	v_mfma_i32_16x16x64_i8 v[134:137], v[118:121], v[190:193], v[134:137]
	s_nop 0
	v_mfma_i32_16x16x64_i8 v[134:137], v[106:109], v[186:189], v[134:137]
	v_mfma_i32_16x16x64_i8 v[130:133], v[102:105], v[190:193], v[130:133]
	s_nop 0
	v_mfma_i32_16x16x64_i8 v[130:133], v[98:101], v[186:189], v[130:133]
	v_mfma_i32_16x16x64_i8 v[114:117], v[118:121], v[182:185], v[114:117]
	s_nop 0
	v_mfma_i32_16x16x64_i8 v[114:117], v[106:109], v[178:181], v[114:117]
	v_mfma_i32_16x16x64_i8 v[110:113], v[102:105], v[182:185], v[110:113]
	s_nop 0
	v_mfma_i32_16x16x64_i8 v[110:113], v[98:101], v[178:181], v[110:113]
	v_mfma_i32_16x16x64_i8 v[86:89], v[118:121], v[174:177], v[86:89]
	s_nop 0
	v_mfma_i32_16x16x64_i8 v[86:89], v[106:109], v[170:173], v[86:89]
	v_mfma_i32_16x16x64_i8 v[82:85], v[102:105], v[174:177], v[82:85]
	s_nop 0
	v_mfma_i32_16x16x64_i8 v[82:85], v[98:101], v[170:173], v[82:85]
	v_mfma_i32_16x16x64_i8 v[70:73], v[118:121], v[166:169], v[70:73]
	s_nop 0
	v_mfma_i32_16x16x64_i8 v[70:73], v[106:109], v[162:165], v[70:73]
	v_mfma_i32_16x16x64_i8 v[66:69], v[102:105], v[166:169], v[66:69]
	s_nop 0
	v_mfma_i32_16x16x64_i8 v[66:69], v[98:101], v[162:165], v[66:69]
	s_setprio 0
	s_barrier
	s_mov_b32 m0, s56
	s_mov_b32 s26, s22
	s_mov_b32 s27, s23
	ds_read_b128 v[190:193], v219 offset:49152
	ds_read_b128 v[186:189], v219 offset:50176
	ds_read_b128 v[182:185], v219 offset:51200
	ds_read_b128 v[178:181], v219 offset:52224
	ds_read_b128 v[174:177], v219 offset:53248
	ds_read_b128 v[170:173], v219 offset:54272
	ds_read_b128 v[166:169], v219 offset:55296
	ds_read_b128 v[162:165], v219 offset:56320
	buffer_load_dwordx4 v210, s[24:27], s4 offen lds
	s_mov_b32 m0, s57
	s_add_i32 s41, s41, 0x84080
	buffer_load_dwordx4 v212, s[24:27], s4 offen lds
	s_mov_b32 m0, s70
	s_andn2_b64 vcc, exec, s[36:37]
	buffer_load_dwordx4 v210, s[24:27], s41 offen lds
	s_mov_b32 m0, s71
	s_nop 0
	buffer_load_dwordx4 v212, s[24:27], s41 offen lds
	s_mov_b32 m0, s68
	s_nop 0
	buffer_load_dwordx4 v1, s[20:23], s93 offen lds
	s_mov_b32 m0, s69
	s_nop 0
	buffer_load_dwordx4 v211, s[20:23], s93 offen lds
	s_waitcnt vmcnt(8)
	s_cbranch_vccnz .LBB0_180
	s_nop 0
	s_nop 0
	s_nop 0
	s_add_i32 s93, s40, s12
	s_add_i32 s4, s93, 0xfffc0000
	s_cmp_lt_u32 s4, 0xfffe0000
	s_cselect_b64 s[40:41], -1, 0
	s_cmp_gt_u32 s4, 0xfffdffff
	s_cselect_b64 s[26:27], -1, 0
	s_cmp_gt_i32 s93, 0x3ffff
	s_mov_b64 s[4:5], s[18:19]
	s_cbranch_scc1 .LBB0_196
	s_and_b64 s[4:5], s[40:41], exec
	s_cselect_b32 s4, 0, 0x4000000
	s_add_u32 s94, s33, s4
	s_addc_u32 s95, s35, 0
	s_add_i32 s96, s93, 0xfffe0000
	s_and_b64 s[4:5], s[40:41], exec
	s_cselect_b32 s40, s93, s96
	s_lshl_b32 s4, s40, 13
	s_ashr_i32 s5, s40, 3
	s_and_b32 s4, s4, 0xc000
	s_ashr_i32 s41, s5, 31
	s_add_u32 s4, s4, s5
	s_addc_u32 s5, 0, s41
	s_lshl_b64 s[4:5], s[4:5], 10
	s_add_u32 s4, s94, s4
	s_addc_u32 s5, s95, s5
	s_lshl_b32 s40, s40, 9
	s_and_b32 s40, s40, 0x200
	s_add_u32 s4, s4, s40
	s_addc_u32 s5, s5, 0
